# v17 + od_nat GEMM walks its units in reverse order (the UT chain and att GEMM that follow start on the tiles it wrote last)
# speedup vs baseline: 1.0010x; 1.0010x over previous
.LBB0_189:
	s_cmp_eq_u32 s54, 15
	v_writelane_b32 v252, s35, 12
	s_cselect_b64 s[0:1], -1, 0
	v_writelane_b32 v252, s0, 13
	s_cmp_eq_u32 s54, 14
	v_mov_b32_e32 v228, 1
	v_writelane_b32 v252, s1, 14
	s_cselect_b64 s[0:1], -1, 0
	v_writelane_b32 v252, s0, 15
	s_cmp_eq_u32 s54, 13
	v_mov_b32_e32 v222, 0x7f7f7f7f
	v_writelane_b32 v252, s1, 16
	s_cselect_b64 s[0:1], -1, 0
	v_writelane_b32 v252, s0, 17
	s_cmp_eq_u32 s54, 12
	v_mov_b32_e32 v186, 0x358637bd
	v_writelane_b32 v252, s1, 18
	s_cselect_b64 s[0:1], -1, 0
	v_writelane_b32 v252, s0, 19
	s_cmp_eq_u32 s54, 11
	v_mov_b32_e32 v224, 0x42800000
	v_writelane_b32 v252, s1, 20
	s_cselect_b64 s[0:1], -1, 0
	v_writelane_b32 v252, s0, 21
	s_cmp_eq_u32 s54, 10
	v_not_b32_e32 v225, 63
	v_writelane_b32 v252, s1, 22
	s_cselect_b64 s[0:1], -1, 0
	v_writelane_b32 v252, s0, 23
	s_cmp_eq_u32 s54, 9
	v_mov_b64_e32 v[230:231], 0x3ff
	v_writelane_b32 v252, s1, 24
	s_cselect_b64 s[0:1], -1, 0
	v_writelane_b32 v252, s0, 25
	s_cmp_eq_u32 s54, 8
	v_mov_b64_e32 v[248:249], 0x400
	v_writelane_b32 v252, s1, 26
	s_cselect_b64 s[0:1], -1, 0
	v_writelane_b32 v252, s0, 27
	s_cmp_eq_u32 s54, 7
	v_mov_b64_e32 v[250:251], 0x1ff
	v_writelane_b32 v252, s1, 28
	s_cselect_b64 s[0:1], -1, 0
	v_writelane_b32 v252, s0, 29
	s_cmp_eq_u32 s54, 6
	v_mov_b32_e32 v187, 0x4ba00000
	v_writelane_b32 v252, s1, 30
	s_cselect_b64 s[0:1], -1, 0
	v_writelane_b32 v252, s0, 31
	s_cmp_eq_u32 s54, 5
	v_mov_b32_e32 v223, 0x4b200000
	v_writelane_b32 v252, s1, 32
	s_cselect_b64 s[0:1], -1, 0
	v_writelane_b32 v252, s0, 33
	s_cmp_eq_u32 s54, 4
	v_mov_b32_e32 v229, 0xf149f2ca
	v_writelane_b32 v252, s1, 34
	s_cselect_b64 s[0:1], -1, 0
	v_writelane_b32 v252, s0, 35
	s_cmp_eq_u32 s54, 3
	s_mov_b32 s37, 0xefa18f08
	v_writelane_b32 v252, s1, 36
	s_cselect_b64 s[0:1], -1, 0
	v_writelane_b32 v252, s0, 37
	s_cmp_eq_u32 s54, 2
	s_mov_b32 s23, 0xc0e00000
	v_writelane_b32 v252, s1, 38
	s_cselect_b64 s[0:1], -1, 0
	v_writelane_b32 v252, s0, 39
	s_cmp_eq_u32 s54, 1
	s_mov_b32 s36, 0x3fb8aa3b
	v_writelane_b32 v252, s1, 40
	s_cselect_b64 s[0:1], -1, 0
	v_writelane_b32 v252, s0, 41
	s_cmp_eq_u32 s54, 0
	s_nop 0
	v_writelane_b32 v252, s1, 42
	s_cselect_b64 s[0:1], -1, 0
	v_writelane_b32 v252, s0, 43
	s_nop 1
	v_writelane_b32 v252, s1, 44
	s_lshl_b32 s0, s54, 6
	s_cmpk_lt_i32 s88, 0x100
	v_writelane_b32 v252, s0, 45
	s_cselect_b64 s[0:1], -1, 0
	v_writelane_b32 v252, s0, 46
	s_cmpk_lt_i32 s88, 0x800
	s_nop 0
	v_writelane_b32 v252, s1, 47
	s_cselect_b64 s[0:1], -1, 0
	v_writelane_b32 v252, s0, 48
	s_nop 1
	v_writelane_b32 v252, s1, 49
	s_ashr_i32 s0, s88, 31
	v_writelane_b32 v252, s0, 50
	s_lshr_b32 s0, s0, 29
	s_add_i32 s0, s88, s0
	v_readlane_b32 s1, v252, 4
	s_ashr_i32 s21, s0, 3
	s_and_b32 s0, s0, -8
	s_lshr_b32 s3, s1, 8
	s_sub_i32 s22, s88, s0
	v_writelane_b32 v252, s3, 51
	s_bfe_u32 s1, s1, 0x20006
	s_lshl_b32 s0, s22, 8
	v_writelane_b32 v252, s1, 52
	s_ashr_i32 s1, s2, 31
	s_cmpk_lt_i32 s88, 0x400
	v_writelane_b32 v252, s1, 53
	s_waitcnt lgkmcnt(0)
	s_cselect_b64 s[4:5], -1, 0
	v_writelane_b32 v252, s4, 54
	s_max_i32 s1, s2, 2
	s_and_b32 s6, s88, 1
	v_writelane_b32 v252, s5, 55
	s_lshr_b32 s4, s1, 1
	v_readlane_b32 s1, v252, 11
	s_and_b32 s1, s1, -16
	s_or_b32 s5, s1, s6
	v_writelane_b32 v252, s5, 56
	s_lshl_b32 s3, s22, 7
	v_writelane_b32 v252, s4, 57
	s_min_i32 s4, s4, 0x80
	s_cmp_gt_i32 s4, s88
	s_cselect_b64 s[4:5], -1, 0
	v_writelane_b32 v252, s4, 58
	s_nop 1
	v_writelane_b32 v252, s5, 59
	s_ashr_i32 s4, s1, 1
	s_ashr_i32 s5, s4, 31
	s_lshl_b64 s[8:9], s[4:5], 19
	v_writelane_b32 v252, s8, 60
	s_lshl_b64 s[4:5], s[4:5], 17
	s_lshl_b32 s1, s6, 17
	v_writelane_b32 v252, s9, 61
	v_writelane_b32 v252, s4, 62
	s_nop 1
	v_writelane_b32 v252, s5, 63
	s_lshr_b32 s4, s2, 31
	s_add_i32 s4, s2, s4
	s_ashr_i32 s4, s4, 1
	s_cmp_gt_i32 s2, 1
	s_cselect_b32 s4, s4, 1
	s_sub_i32 s8, s2, s4
	s_sub_i32 s9, s88, s4
	s_cmp_ge_i32 s88, s4
	s_cselect_b64 s[4:5], -1, 0
	s_and_b64 s[6:7], s[4:5], exec
	s_cselect_b32 s10, s8, 1
	s_cselect_b32 s11, s9, 0
	s_cmp_lt_i32 s2, 2
	s_cselect_b64 s[6:7], -1, 0
	s_and_b64 s[8:9], s[6:7], exec
	s_cselect_b32 s8, 1, s10
	s_cselect_b32 s9, 0, s11
	s_or_b64 s[4:5], s[6:7], s[4:5]
	s_and_b64 s[4:5], s[4:5], exec
	s_cselect_b32 s24, 0x200, 0
	s_cmp_lt_i32 s9, s24
	s_cselect_b64 s[4:5], -1, 0
	v_writelane_b32 v253, s4, 0
	s_lshr_b32 s16, s24, 3
	s_or_b32 s17, s16, 1
	v_writelane_b32 v253, s5, 1
	s_ashr_i32 s4, s9, 31
	v_writelane_b32 v253, s4, 2
	s_lshr_b32 s4, s4, 29
	s_add_i32 s4, s9, s4
	s_ashr_i32 s6, s4, 3
	s_and_b32 s4, s4, -8
	v_writelane_b32 v253, s9, 3
	s_sub_i32 s7, s9, s4
	s_ashr_i32 s4, s8, 31
	s_lshl_b32 s34, s2, 4
	v_writelane_b32 v253, s8, 4
	s_cmpk_lt_i32 s88, 0x200
	v_writelane_b32 v253, s4, 5
	s_cselect_b64 s[4:5], -1, 0
	v_writelane_b32 v253, s4, 6
	s_mul_i32 s10, s22, 0x41
	s_mul_i32 s11, s22, 5
	v_writelane_b32 v253, s5, 7
	s_lshl_b32 s4, s22, 6
	s_cmpk_lt_i32 s88, 0x180
	s_cselect_b64 s[8:9], -1, 0
	v_writelane_b32 v253, s8, 8
	s_cmp_lt_i32 s88, 32
	s_nop 0
	v_writelane_b32 v253, s9, 9
	s_cselect_b64 s[8:9], -1, 0
	v_writelane_b32 v253, s8, 10
	s_lshl_b32 s5, s22, 2
	s_nop 0
	v_writelane_b32 v253, s9, 11
	s_lshl_b32 s8, s88, 9
	v_writelane_b32 v253, s8, 12
	s_lshl_b32 s8, s2, 9
	v_writelane_b32 v253, s8, 13
	s_cmp_lt_i32 s22, 0
	s_mul_i32 s8, s22, 0x101
	s_mul_i32 s9, s22, 0x81
	s_cselect_b32 s0, s8, s0
	s_cselect_b32 s8, s9, s3
	s_cselect_b32 s9, s10, s4
	s_cselect_b32 s10, 49, 48
	s_cselect_b32 s3, s11, s5
	s_add_i32 s0, s0, s21
	s_sub_i32 s0, 0x7ff, s0
	s_ashr_i32 s4, s0, 31
	s_lshr_b32 s4, s4, 25
	s_add_i32 s4, s0, s4
	s_ashr_i32 s5, s0, 5
	s_and_b32 s4, s0, 31
	s_and_b32 s11, s4, 1
	s_lshr_b32 s12, s4, 1
	s_nop 0
	s_nop 0
	s_nop 0
	s_nop 0
	s_nop 0
	s_lshl_b32 s5, s5, 1
	s_nop 0
	s_nop 0
	s_add_i32 s8, s8, s21
	s_add_i32 s26, s5, s11
	s_mov_b32 s4, s12
	s_ashr_i32 s11, s8, 31
	v_writelane_b32 v253, s4, 14
	s_lshr_b32 s4, s11, 22
	s_add_i32 s4, s8, s4
	s_ashr_i32 s5, s4, 10
	s_and_b32 s4, s4, 0xfc00
	s_sub_i32 s4, s8, s4
	s_mov_b32 s0, s12
	s_sext_i32_i16 s12, s4
	s_bfe_u32 s12, s12, 0x3001c
	s_add_i32 s12, s4, s12
	s_sext_i32_i16 s13, s12
	s_and_b32 s12, s12, 0xfff8
	s_sub_i32 s12, s4, s12
	s_lshl_b32 s5, s5, 3
	s_sext_i32_i16 s12, s12
	s_lshr_b32 s4, s13, 3
	s_add_i32 s12, s5, s12
	s_ashr_i32 s5, s13, 3
	v_writelane_b32 v253, s5, 15
	s_bfe_i64 s[4:5], s[4:5], 0x100000
	s_lshl_b64 s[4:5], s[4:5], 18
	v_writelane_b32 v253, s4, 16
	s_ashr_i32 s13, s12, 31
	s_mul_i32 s10, s22, s10
	v_writelane_b32 v253, s5, 17
	s_mov_b32 s4, s12
	v_writelane_b32 v253, s4, 18
	s_nop 1
	v_writelane_b32 v253, s5, 19
	s_lshl_b64 s[4:5], s[12:13], 18
	v_writelane_b32 v253, s4, 20
	s_cmp_lt_i32 s7, 0
	s_cselect_b32 s12, s17, s16
	v_writelane_b32 v253, s5, 21
	s_lshr_b32 s4, s11, 28
	s_add_i32 s4, s8, s4
	s_and_b32 s5, s4, 0xfff0
	s_sub_i32 s5, s8, s5
	s_bfe_i32 s13, s5, 0x80000
	s_bfe_u32 s13, s13, 0x3000c
	s_mul_i32 s7, s12, s7
	s_add_i32 s13, s5, s13
	s_add_i32 s6, s7, s6
	s_add_i32 s7, s9, s21
	v_writelane_b32 v253, s16, 22
	s_and_b32 s16, s13, 0xf8
	s_ashr_i32 s9, s7, 31
	s_sub_i32 s16, s5, s16
	s_ashr_i32 s4, s4, 4
	s_lshr_b32 s9, s9, 27
	s_lshl_b32 s4, s4, 3
	s_sext_i32_i8 s5, s16
	s_add_i32 s9, s7, s9
	s_add_i32 s28, s4, s5
	s_and_b32 s12, s9, 0xffe0
	s_ashr_i32 s4, s28, 5
	s_sub_i32 s7, s7, s12
	s_ashr_i32 s5, s4, 31
	s_lshl_b32 s16, s16, 10
	s_bfe_i32 s12, s7, 0x80000
	s_and_b32 s16, s16, 0x1c00
	s_lshl_b64 s[4:5], s[4:5], 13
	s_bfe_u32 s12, s12, 0x3000c
	s_or_b32 s4, s4, s16
	s_bfe_u32 s16, s28, 0x20003
	s_add_i32 s12, s7, s12
	s_lshr_b32 s11, s11, 26
	s_or_b32 s4, s4, s16
	s_and_b32 s16, s12, 0xf8
	s_add_i32 s11, s8, s11
	s_sub_i32 s7, s7, s16
	s_and_b32 s16, s11, 0xffe0
	s_sub_i32 s8, s8, s16
	s_bfe_i32 s16, s8, 0x80000
	s_bfe_u32 s16, s16, 0x3000c
	s_add_i32 s16, s8, s16
	v_writelane_b32 v253, s17, 23
	s_and_b32 s17, s16, 0xfc
	s_add_i32 s10, s10, s21
	s_sub_i32 s8, s8, s17
	s_ashr_i32 s17, s10, 31
	s_lshr_b32 s17, s17, 22
	s_add_i32 s17, s10, s17
	s_and_b32 s18, s17, 0xfffffc00
	s_sub_i32 s10, s10, s18
	s_ashr_i32 s18, s6, 31
	s_lshr_b32 s18, s18, 29
	s_add_i32 s18, s6, s18
	s_and_b32 s18, s18, -8
	s_sub_i32 s20, s6, s18
	s_bfe_i32 s6, s13, 0x80000
	s_lshl_b64 s[4:5], s[4:5], 10
	s_sext_i32_i16 s6, s6
	v_writelane_b32 v253, s4, 24
	s_sext_i32_i8 s8, s8
	s_ashr_i32 s29, s28, 31
	v_writelane_b32 v253, s5, 25
	s_ashr_i32 s4, s6, 3
	v_writelane_b32 v253, s4, 26
	s_lshr_b32 s4, s6, 3
	s_bfe_i64 s[4:5], s[4:5], 0x100000
	s_lshl_b64 s[4:5], s[4:5], 18
	v_writelane_b32 v253, s4, 27
	s_sext_i32_i8 s6, s7
	s_bfe_i32 s7, s16, 0x80000
	v_writelane_b32 v253, s5, 28
	s_ashr_i32 s4, s9, 5
	s_bfe_i32 s5, s12, 0x80000
	s_lshl_b32 s4, s4, 3
	s_sext_i32_i16 s5, s5
	s_add_i32 s30, s4, s6
	s_ashr_i32 s4, s5, 3
	v_writelane_b32 v253, s4, 29
	s_ashr_i32 s6, s11, 5
	s_sext_i32_i16 s7, s7
	s_lshl_b32 s6, s6, 2
	v_writelane_b32 v253, s21, 30
	s_add_i32 s9, s3, s21
	s_ashr_i32 s3, s7, 2
	s_add_i32 s16, s6, s8
	v_writelane_b32 v253, s3, 31
	s_mov_b32 s8, s28
	v_writelane_b32 v253, s8, 32
	s_lshl_b64 s[28:29], s[28:29], 19
	s_ashr_i32 s31, s30, 31
	v_writelane_b32 v253, s9, 33
	s_ashr_i32 s6, s17, 10
	v_writelane_b32 v253, s28, 34
	s_lshr_b32 s4, s5, 3
	s_lshl_b32 s11, s6, 3
	v_writelane_b32 v253, s29, 35
	s_lshl_b64 s[28:29], s[30:31], 19
	s_sub_i32 s19, s24, s18
	s_bfe_i64 s[4:5], s[4:5], 0x100000
	s_sub_i32 s6, 3, s11
	v_writelane_b32 v253, s28, 36
	s_min_i32 s19, s19, 8
	s_min_u32 s12, s6, 8
	s_lshr_b32 s6, s7, 2
	v_writelane_b32 v253, s29, 37
	s_lshl_b64 s[28:29], s[4:5], 19
	v_writelane_b32 v253, s28, 38
	s_cmp_lt_u32 s9, 16
	v_cvt_f32_i32_e32 v1, s20
	v_writelane_b32 v253, s29, 39
	s_cselect_b64 s[28:29], -1, 0
	v_writelane_b32 v253, s28, 40
	s_ashr_i32 s8, s9, 4
	s_lshl_b32 s3, s9, 18
	v_writelane_b32 v253, s29, 41
	v_writelane_b32 v253, s9, 42
	s_ashr_i32 s9, s8, 31
	s_lshl_b64 s[8:9], s[8:9], 20
	v_writelane_b32 v253, s8, 43
	s_ashr_i32 s27, s26, 31
	s_ashr_i32 s17, s16, 31
	v_writelane_b32 v253, s9, 44
	s_lshl_b64 s[8:9], s[4:5], 18
	v_writelane_b32 v253, s8, 45
	s_lshl_b64 s[4:5], s[4:5], 17
	s_and_b32 s3, s3, 0x3c0000
	v_writelane_b32 v253, s9, 46
	v_writelane_b32 v253, s4, 47
	s_mov_b32 s29, 0
	s_mov_b32 s25, s29
	v_writelane_b32 v253, s5, 48
	s_bfe_i64 s[4:5], s[0:1], 0x100000
	s_lshl_b64 s[4:5], s[4:5], 18
	v_writelane_b32 v253, s4, 49
	s_sext_i32_i16 s0, s19
	v_cvt_f32_i32_e32 v0, s0
	v_writelane_b32 v253, s5, 50
	s_bfe_i64 s[4:5], s[6:7], 0x100000
	s_lshl_b64 s[4:5], s[4:5], 19
	v_writelane_b32 v253, s4, 51
	v_rcp_iflag_f32_e32 v2, v0
	s_mov_b32 s19, 0xf149f2ca
	v_writelane_b32 v253, s5, 52
	s_xor_b32 s4, s20, s0
	s_ashr_i32 s4, s4, 30
	s_or_b32 s6, s4, 1
	v_writelane_b32 v253, s22, 53
	s_lshr_b32 s4, s22, 31
	v_writelane_b32 v253, s4, 54
	s_lshl_b64 s[4:5], s[30:31], 18
	v_writelane_b32 v253, s4, 55
	v_mul_f32_e32 v2, v1, v2
	v_trunc_f32_e32 v2, v2
	v_writelane_b32 v253, s5, 56
	s_mov_b32 s4, s30
	v_writelane_b32 v253, s4, 57
	v_fma_f32 v1, -v2, v0, v1
	s_mov_b32 s22, 0x3d000000
	v_writelane_b32 v253, s5, 58
	s_lshl_b64 s[4:5], s[30:31], 17
	v_writelane_b32 v253, s4, 59
	s_mov_b32 s30, 0xc01d265f
	s_nop 0
	v_writelane_b32 v253, s5, 60
	s_mov_b32 s4, s26
	v_writelane_b32 v253, s4, 61
	s_nop 1
	v_writelane_b32 v253, s5, 62
	s_lshl_b64 s[4:5], s[26:27], 18
	v_writelane_b32 v253, s4, 63
	s_mov_b32 s26, 0x3b800000
	s_nop 0
	v_writelane_b32 v254, s5, 0
	s_mov_b32 s4, s16
	v_writelane_b32 v254, s4, 1
	s_nop 1
	v_writelane_b32 v254, s5, 2
	s_lshl_b64 s[4:5], s[16:17], 19
	v_writelane_b32 v254, s4, 3
	s_mov_b32 s17, 0x800000
	s_mov_b32 s16, 0x3b000000
	v_writelane_b32 v254, s5, 4
	v_cmp_ge_f32_e64 s[4:5], |v1|, |v0|
	v_cvt_i32_f32_e32 v0, v2
	s_and_b64 s[4:5], s[4:5], exec
	s_cselect_b32 s4, s6, 0
	v_cvt_f32_ubyte0_e32 v1, s12
	v_readfirstlane_b32 s5, v0
	s_add_i32 s4, s5, s4
	s_mul_i32 s4, s4, s0
	s_sub_i32 s0, s20, s4
	s_sext_i32_i16 s4, s0
	s_add_i32 s9, s18, s4
	s_ashr_i32 s4, s9, 5
	s_ashr_i32 s5, s4, 31
	s_lshl_b32 s6, s0, 10
	s_and_b32 s8, s6, 0x1c00
	s_lshl_b64 s[6:7], s[4:5], 13
	s_or_b32 s6, s6, s8
	s_bfe_u32 s8, s9, 0x20003
	s_or_b32 s6, s6, s8
	v_cvt_f32_i32_e32 v0, s10
	v_rcp_iflag_f32_e32 v2, v1
	s_lshl_b64 s[6:7], s[6:7], 10
	v_writelane_b32 v254, s6, 5
	s_lshl_b64 s[4:5], s[4:5], 22
	v_mul_f32_e32 v2, v0, v2
	v_writelane_b32 v254, s7, 6
	v_writelane_b32 v254, s4, 7
	v_trunc_f32_e32 v2, v2
	v_fma_f32 v0, -v2, v1, v0
	v_writelane_b32 v254, s5, 8
	s_lshl_b32 s4, s9, 5
	s_and_b32 s6, s4, 0x300
	s_ashr_i32 s4, s10, 30
	s_or_b32 s7, s4, 1
	v_cmp_ge_f32_e64 s[4:5], |v0|, v1
	v_cvt_i32_f32_e32 v0, v2
	s_lshl_b32 s0, s0, 18
	s_and_b32 s0, s0, 0x1c0000
	s_and_b64 s[4:5], s[4:5], exec
	s_cselect_b32 s4, s7, 0
	v_readfirstlane_b32 s5, v0
	s_add_i32 s4, s5, s4
	s_mul_i32 s5, s4, s12
	s_sub_i32 s5, s10, s5
	s_sext_i32_i16 s5, s5
	v_writelane_b32 v254, s9, 9
	s_add_i32 s5, s11, s5
	v_writelane_b32 v254, s5, 10
	s_abs_i32 s5, s2
	v_cvt_f32_u32_e32 v0, s5
	v_writelane_b32 v254, s5, 11
	s_sub_i32 s5, 0, s5
	s_sext_i32_i16 s4, s4
	v_rcp_iflag_f32_e32 v0, v0
	s_lshl_b32 s1, s1, 1
	s_lshl_b32 s0, s0, 1
	s_ashr_i32 s35, s34, 31
	v_mul_f32_e32 v0, 0x4f7ffffe, v0
	v_cvt_u32_f32_e32 v0, v0
	v_mov_b32_e32 v1, 0
	s_add_i32 s31, 0, 0x23600
	s_mov_b32 s18, 0xbd38aa3b
	v_readfirstlane_b32 s7, v0
	s_mul_i32 s5, s5, s7
	s_mul_hi_u32 s5, s7, s5
	s_add_i32 s5, s7, s5
	v_writelane_b32 v254, s5, 12
	v_writelane_b32 v254, s24, 13
	s_nop 1
	v_writelane_b32 v254, s25, 14
	v_writelane_b32 v254, s4, 15
	v_writelane_b32 v254, s1, 16
	v_writelane_b32 v254, s0, 17
	s_lshl_b32 s0, s6, 1
	v_writelane_b32 v254, s0, 18
	s_lshl_b32 s0, s3, 1
	v_writelane_b32 v254, s0, 19
	s_lshl_b32 s0, s88, 7
	v_writelane_b32 v254, s0, 20
	s_lshl_b32 s0, s2, 7
	v_writelane_b32 v254, s0, 21
	s_lshl_b32 s0, s88, 5
	v_writelane_b32 v254, s0, 22
	s_lshl_b32 s0, s2, 5
	v_writelane_b32 v254, s0, 23
	s_add_i32 s0, 0, 0x22000
	v_writelane_b32 v254, s0, 24
	s_add_i32 s0, 0, 0x22004
	v_writelane_b32 v254, s0, 25
	s_add_i32 s0, 0, 0x22d10
	v_writelane_b32 v254, s0, 26
	s_add_i32 s0, 0, 0x22d20
	v_writelane_b32 v254, s0, 27
	s_add_i32 s0, 0, 0x22d30
	v_writelane_b32 v254, s0, 28
	s_add_i32 s0, 0, 0x22d40
	v_writelane_b32 v254, s0, 29
	s_add_i32 s0, 0, 0x22d50
	v_writelane_b32 v254, s0, 30
	s_add_i32 s0, 0, 0x22d60
	v_writelane_b32 v254, s0, 31
	s_add_i32 s0, 0, 0x22d70
	v_writelane_b32 v254, s0, 32
	s_add_i32 s0, 0, 0x22500
	v_writelane_b32 v254, s0, 33
	s_add_i32 s0, 0, 0x23500
	v_writelane_b32 v254, s0, 34
	s_add_i32 s0, 0, 0x22d80
	v_writelane_b32 v254, s0, 35
	s_add_i32 s0, 0, 0x22d90
	v_writelane_b32 v254, s0, 36
	s_add_i32 s0, 0, 0x22da0
	v_writelane_b32 v254, s0, 37
	s_add_i32 s0, 0, 0x22db0
	v_writelane_b32 v254, s0, 38
	s_add_i32 s0, 0, 0x22dc0
	v_writelane_b32 v254, s0, 39
	s_add_i32 s0, 0, 0x22dd0
	v_writelane_b32 v254, s0, 40
	s_add_i32 s0, 0, 0x22de0
	v_writelane_b32 v254, s0, 41
	s_add_i32 s0, 0, 0x22df0
	v_writelane_b32 v254, s0, 42
	s_add_i32 s0, 0, 0x22100
	v_writelane_b32 v254, s0, 43
	s_add_i32 s0, 0, 0x23510
	v_writelane_b32 v254, s0, 44
	s_add_i32 s0, 0, 0x23610
	v_writelane_b32 v254, s0, 45
	s_add_i32 s0, 0, 0x23520
	v_writelane_b32 v254, s0, 46
	s_add_i32 s0, 0, 0x23620
	v_writelane_b32 v254, s0, 47
	s_add_i32 s0, 0, 0x23530
	v_writelane_b32 v254, s0, 48
	s_add_i32 s0, 0, 0x23630
	v_writelane_b32 v254, s0, 49
	s_add_i32 s0, 0, 0x23540
	v_writelane_b32 v254, s0, 50
	s_add_i32 s0, 0, 0x23640
	v_writelane_b32 v254, s0, 51
	s_add_i32 s0, 0, 0x23550
	v_writelane_b32 v254, s0, 52
	s_add_i32 s0, 0, 0x23650
	v_writelane_b32 v254, s0, 53
	s_add_i32 s0, 0, 0x23560
	v_writelane_b32 v254, s0, 54
	s_add_i32 s0, 0, 0x23660
	v_writelane_b32 v254, s0, 55
	s_add_i32 s0, 0, 0x23570
	v_writelane_b32 v254, s0, 56
	s_add_i32 s0, 0, 0x23670
	v_writelane_b32 v254, s0, 57
	s_add_i32 s0, 0, 0x23680
	v_writelane_b32 v254, s0, 58
	s_lshl_b64 s[4:5], s[34:35], 11
	v_writelane_b32 v254, s4, 59
	s_movk_i32 s1, 0x200
	s_add_i32 s3, 0, 0x24a00
	v_writelane_b32 v254, s5, 60
	s_lshl_b64 s[4:5], s[34:35], 10
	v_writelane_b32 v254, s4, 61
	s_mov_b64 s[24:25], 0x80
	s_mov_b32 s0, 0x3e000000
	v_writelane_b32 v254, s5, 62
	s_mov_b32 s4, s88
	v_writelane_b32 v254, s4, 63
	s_mov_b32 s6, s29
	s_nop 0
	v_writelane_b32 v255, s5, 0
	v_writelane_b32 v255, s34, 1
	s_nop 1
	v_writelane_b32 v255, s35, 2
	s_branch .LBB0_193

.LBB0_373:
	s_ashr_i32 s12, s28, 3
	s_add_i32 s12, s43, s12
	s_sub_i32 s12, 0x7ff, s12
	s_ashr_i32 s13, s12, 31
	s_lshr_b32 s13, s13, 27
	s_add_i32 s13, s12, s13
	s_ashr_i32 s28, s13, 5
	s_lshl_b32 s28, s28, 1
	s_sub_i32 s42, 0x80, s28
	s_min_i32 s43, s42, 2
	s_abs_i32 s42, s43
	v_cvt_f32_u32_e32 v2, s42
	s_sub_i32 s45, 0, s42
	s_and_b32 s13, s13, 0xffffffe0
	s_sub_i32 s12, s12, s13
	v_rcp_iflag_f32_e32 v2, v2
	s_abs_i32 s13, s12
	s_xor_b32 s44, s12, s43
	s_ashr_i32 s44, s44, 31
	v_mul_f32_e32 v2, 0x4f7ffffe, v2
	v_cvt_u32_f32_e32 v2, v2
	s_nop 0
	v_readfirstlane_b32 s47, v2
	s_mul_i32 s45, s45, s47
	s_mul_hi_u32 s45, s47, s45
	s_add_i32 s47, s47, s45
	s_mul_hi_u32 s45, s13, s47
	s_mul_i32 s47, s45, s42
	s_sub_i32 s13, s13, s47
	s_add_i32 s48, s45, 1
	s_sub_i32 s47, s13, s42
	s_cmp_ge_u32 s13, s42
	s_cselect_b32 s45, s48, s45
	s_cselect_b32 s13, s47, s13
	s_add_i32 s47, s45, 1
	s_cmp_ge_u32 s13, s42
	s_cselect_b32 s13, s47, s45
	s_xor_b32 s13, s13, s44
	s_sub_i32 s42, s13, s44
	s_mul_i32 s13, s42, s43
	s_sub_i32 s12, s12, s13
	s_add_i32 s44, s28, s12
